# C2: software L2 prefetch of the next unit's expert-weight tile (K-tiles 2..7) at the start of the epilogue
# speedup vs baseline: 1.0071x; 1.0058x over previous
; #define LAS __attribute__((address_space(3)))
; template <bool EMU> __device__ __forceinline__ float e2m3q(float y) { if constexpr (EMU) { y = fminf(fmaxf(y, -7.5f), 7.5f); return fabsf(y) < 1.f ? rintf(y * 8.f) * 0.125f : y; } else return y; }
;     __device__ __forceinline__ void operator()(const f32x4 (&acc)[2][2][4][2], const UnitD& u, int wr, int wc, int fr, int fq) const {
;         const int row0 = u.r0 + wr * 64 + fr, col0 = u.c0 + wc * 32 + 8 * fq;
;         const LAS float* bg = bl_lds + u.ui * 256 + wc * 32 + 8 * fq; const LAS float* bl = bg + 128;
;         f32x4 bgv[2], blv[2];
; #pragma unroll
;         for (int n = 0; n < 2; ++n) { bgv[n] = *(const LAS f32x4*)(bg + 4 * n); blv[n] = *(const LAS f32x4*)(bl + 4 * n); }
;         constexpr float SC = 1.f / (QS_X1 * QS_WUP);
; #pragma unroll
;         for (int ai = 0; ai < 2; ++ai)
; #pragma unroll
;             for (int m = 0; m < 4; ++m) { unsigned char* rowp = H + (size_t)(row0 + ai * 128 + m * 16) * DM + col0; u32x2 w;
; #pragma unroll
;                 for (int n = 0; n < 2; ++n) { const f32x4 g = acc[ai][0][m][n] * SC + bgv[n], l = acc[ai][1][m][n] * SC + blv[n];
;                     const f32x2 o0 = act2((f32x2){g[0], g[1]}, (f32x2){l[0], l[1]}), o1 = act2((f32x2){g[2], g[3]}, (f32x2){l[2], l[3]});
;                     int r = 0; r = __builtin_amdgcn_cvt_pk_fp8_f32(e2m3q<EMU_DOWN != 0>(o0.x), e2m3q<EMU_DOWN != 0>(o0.y), r, false); r = __builtin_amdgcn_cvt_pk_fp8_f32(e2m3q<EMU_DOWN != 0>(o1.x), e2m3q<EMU_DOWN != 0>(o1.y), r, true);
;                     if (n == 0) w.x = (unsigned)r; else w.y = (unsigned)r; }
.LBB0_755:
	s_add_u32 s18, s85, 0xffffff00
	v_mov_b32_e32 v16, v154
	v_bfe_u32 v152, v154, 4, 1
	s_addc_u32 s19, s86, -1
	s_lshl_b32 s20, s76, 10
	v_mul_u32_u24_e32 v152, 0x3ff8, v152
	v_lshrrev_b32_e32 v0, 1, v16
	v_and_b32_e32 v18, 0x60, v0
	v_and_b32_e32 v19, 24, v0
	s_add_i32 s20, s20, 0
	s_add_i32 s20, s20, 0x23100
	v_lshlrev_b32_e32 v0, 2, v18
	v_lshlrev_b32_e32 v1, 2, v19
	v_add3_u32 v4, s20, v0, v1
	s_mov_b32 s20, s90
	s_mov_b32 s21, s89
	v_and_b32_e32 v216, 0x7f, v154
	v_bfe_u32 v217, v154, 7, 1
	v_lshrrev_b32_e32 v218, 8, v154
	v_lshlrev_b32_e32 v216, 10, v216
	v_lshl_add_u32 v216, v217, 20, v216
	v_mul_u32_u24_e32 v218, 0x180, v218
	v_add_u32_e32 v216, v216, v218
	s_nop 0
	global_load_dword v217, v216, s[20:21] offset:256
	global_load_dword v218, v216, s[20:21] offset:384
	global_load_dword v219, v216, s[20:21] offset:512
	ds_read_b128 v[8:11], v4
	ds_read_b128 v[0:3], v4 offset:16
	ds_read_b128 v[12:15], v4 offset:512
	ds_read_b128 v[4:7], v4 offset:528
	v_and_b32_e32 v17, 15, v16
	s_waitcnt lgkmcnt(0)
	v_pk_fma_f32 v[22:23], v[148:149], s[36:37], v[8:9] op_sel_hi:[1,0,1]
	v_ashrrev_i32_e32 v20, 2, v16
	v_min_f32_e32 v23, 0x40e00000, v23
	v_min_f32_e32 v22, 0x40e00000, v22
	v_pk_mul_f32 v[176:177], v[22:23], s[78:79] op_sel_hi:[1,0]
	v_pk_fma_f32 v[174:175], v[116:117], s[36:37], v[12:13] op_sel_hi:[1,0,1]
	v_exp_f32_e32 v176, v176
	v_exp_f32_e32 v177, v177
	v_and_or_b32 v17, v20, s39, v17
	v_pk_fma_f32 v[20:21], v[150:151], s[36:37], v[10:11] op_sel_hi:[1,0,1]
	v_med3_f32 v175, v175, s47, v190
	v_pk_add_f32 v[176:177], v[176:177], 1.0 op_sel_hi:[1,0]
	v_med3_f32 v174, v174, s47, v190
	v_rcp_f32_e32 v176, v176
	v_rcp_f32_e32 v177, v177
	v_pk_fma_f32 v[174:175], v[174:175], 4.0, 4.0 op_sel_hi:[1,0,0]
	v_min_f32_e32 v21, 0x40e00000, v21
	v_min_f32_e32 v20, 0x40e00000, v20
	v_pk_mul_f32 v[22:23], v[22:23], v[176:177]
	v_pk_fma_f32 v[172:173], v[118:119], s[36:37], v[14:15] op_sel_hi:[1,0,1]
	v_pk_mul_f32 v[22:23], v[174:175], v[22:23]
	v_pk_mul_f32 v[174:175], v[20:21], s[78:79] op_sel_hi:[1,0]
	v_med3_f32 v173, v173, s47, v190
	v_exp_f32_e32 v174, v174
	v_exp_f32_e32 v175, v175
	v_med3_f32 v172, v172, s47, v190
	v_pk_fma_f32 v[172:173], v[172:173], 4.0, 4.0 op_sel_hi:[1,0,0]
	v_pk_fma_f32 v[176:177], v[112:113], s[36:37], v[4:5] op_sel_hi:[1,0,1]
	v_pk_add_f32 v[174:175], v[174:175], 1.0 op_sel_hi:[1,0]
	v_med3_f32 v177, v177, s47, v190
	v_rcp_f32_e32 v174, v174
	v_rcp_f32_e32 v175, v175
	v_med3_f32 v176, v176, s47, v190
	v_pk_fma_f32 v[176:177], v[176:177], 4.0, 4.0 op_sel_hi:[1,0,0]
	v_add3_u32 v16, v18, s2, v19
	v_pk_mul_f32 v[20:21], v[20:21], v[174:175]
	v_pk_fma_f32 v[174:175], v[114:115], s[36:37], v[6:7] op_sel_hi:[1,0,1]
	v_pk_mul_f32 v[20:21], v[172:173], v[20:21]
	v_cvt_pk_fp8_f32 v148, v22, v23
	v_pk_fma_f32 v[22:23], v[144:145], s[36:37], v[0:1] op_sel_hi:[1,0,1]
	v_min_f32_e32 v23, 0x40e00000, v23
	v_min_f32_e32 v22, 0x40e00000, v22
	v_pk_mul_f32 v[178:179], v[22:23], s[78:79] op_sel_hi:[1,0]
	v_cvt_pk_fp8_f32 v148, v20, v21 op_sel:[0,0,1]
	v_exp_f32_e32 v178, v178
	v_exp_f32_e32 v179, v179
	v_pk_fma_f32 v[20:21], v[146:147], s[36:37], v[2:3] op_sel_hi:[1,0,1]
	v_med3_f32 v175, v175, s47, v190
	v_min_f32_e32 v21, 0x40e00000, v21
	v_pk_add_f32 v[178:179], v[178:179], 1.0 op_sel_hi:[1,0]
	v_min_f32_e32 v20, 0x40e00000, v20
	v_rcp_f32_e32 v178, v178
	v_rcp_f32_e32 v179, v179
	v_med3_f32 v174, v174, s47, v190
	v_pk_fma_f32 v[174:175], v[174:175], 4.0, 4.0 op_sel_hi:[1,0,0]
	v_add_u32_e32 v18, s68, v17
	v_pk_mul_f32 v[22:23], v[22:23], v[178:179]
	v_ashrrev_i32_e32 v19, 31, v18
	v_pk_mul_f32 v[22:23], v[176:177], v[22:23]
	v_pk_mul_f32 v[176:177], v[20:21], s[78:79] op_sel_hi:[1,0]
	v_cvt_pk_fp8_f32 v149, v22, v23
	v_exp_f32_e32 v176, v176
	v_exp_f32_e32 v177, v177
	v_lshlrev_b64 v[18:19], 10, v[18:19]
	v_ashrrev_i32_e32 v17, 31, v16
	v_lshl_add_u64 v[18:19], s[6:7], 0, v[18:19]
	v_pk_add_f32 v[176:177], v[176:177], 1.0 op_sel_hi:[1,0]
	v_lshl_add_u64 v[16:17], v[18:19], 0, v[16:17]
	s_nop 0
	v_lshl_add_u64 v[144:145], v[16:17], 0, v[152:153]
	v_rcp_f32_e32 v176, v176
	v_rcp_f32_e32 v177, v177
	v_pk_fma_f32 v[18:19], v[142:143], s[36:37], v[10:11] op_sel_hi:[1,0,1]
	v_pk_fma_f32 v[22:23], v[110:111], s[36:37], v[14:15] op_sel_hi:[1,0,1]
	v_min_f32_e32 v19, 0x40e00000, v19
	v_pk_mul_f32 v[20:21], v[20:21], v[176:177]
	v_min_f32_e32 v18, 0x40e00000, v18
	v_pk_mul_f32 v[20:21], v[174:175], v[20:21]
	v_med3_f32 v23, v23, s47, v190
	v_cvt_pk_fp8_f32 v149, v20, v21 op_sel:[0,0,1]
	v_pk_fma_f32 v[20:21], v[140:141], s[36:37], v[8:9] op_sel_hi:[1,0,1]
	v_med3_f32 v22, v22, s47, v190
	v_min_f32_e32 v21, 0x40e00000, v21
	v_min_f32_e32 v20, 0x40e00000, v20
	v_pk_mul_f32 v[174:175], v[20:21], s[78:79] op_sel_hi:[1,0]
	v_exp_f32_e32 v174, v174
	v_exp_f32_e32 v175, v175
	v_pk_fma_f32 v[172:173], v[108:109], s[36:37], v[12:13] op_sel_hi:[1,0,1]
	v_pk_fma_f32 v[22:23], v[22:23], 4.0, 4.0 op_sel_hi:[1,0,0]
	v_med3_f32 v173, v173, s47, v190
	v_pk_add_f32 v[174:175], v[174:175], 1.0 op_sel_hi:[1,0]
	v_med3_f32 v172, v172, s47, v190
	v_rcp_f32_e32 v174, v174
	v_rcp_f32_e32 v175, v175
	v_pk_fma_f32 v[172:173], v[172:173], 4.0, 4.0 op_sel_hi:[1,0,0]
	s_movk_i32 s20, 0x4000
	s_mov_b64 s[88:89], 0x42040080
	v_pk_mul_f32 v[20:21], v[20:21], v[174:175]
	v_pk_fma_f32 v[174:175], v[104:105], s[36:37], v[4:5] op_sel_hi:[1,0,1]
	v_pk_mul_f32 v[20:21], v[172:173], v[20:21]
	v_pk_mul_f32 v[172:173], v[18:19], s[78:79] op_sel_hi:[1,0]
	v_med3_f32 v175, v175, s47, v190
	v_exp_f32_e32 v172, v172
	v_exp_f32_e32 v173, v173
	v_med3_f32 v174, v174, s47, v190
	v_pk_fma_f32 v[174:175], v[174:175], 4.0, 4.0 op_sel_hi:[1,0,0]
	v_pk_add_f32 v[172:173], v[172:173], 1.0 op_sel_hi:[1,0]
; #define LAS __attribute__((address_space(3)))
; template <bool EMU> __device__ __forceinline__ float e2m3q(float y) { if constexpr (EMU) { y = fminf(fmaxf(y, -7.5f), 7.5f); return fabsf(y) < 1.f ? rintf(y * 8.f) * 0.125f : y; } else return y; }
;     static __device__ __forceinline__ f32x2 act2(f32x2 g, f32x2 l) {
;         g = __builtin_elementwise_min(g, (f32x2){7.f, 7.f}); l = __builtin_elementwise_min(__builtin_elementwise_max(l, (f32x2){-7.f, -7.f}), (f32x2){7.f, 7.f});
;         const f32x2 t = g * (-1.702f * 1.44269504089f); f32x2 e; e.x = __builtin_amdgcn_exp2f(t.x); e.y = __builtin_amdgcn_exp2f(t.y);
;         const f32x2 d = e + 1.0f; f32x2 r; r.x = __builtin_amdgcn_rcpf(d.x); r.y = __builtin_amdgcn_rcpf(d.y);
;         return (g * r) * (l * QS_ACT + QS_ACT);
;     }
;     __device__ __forceinline__ void operator()(const f32x4 (&acc)[2][2][4][2], const UnitD& u, int wr, int wc, int fr, int fq) const {
;         const int row0 = u.r0 + wr * 64 + fr, col0 = u.c0 + wc * 32 + 8 * fq;
;         const LAS float* bg = bl_lds + u.ui * 256 + wc * 32 + 8 * fq; const LAS float* bl = bg + 128;
;         f32x4 bgv[2], blv[2];
; #pragma unroll
;         for (int n = 0; n < 2; ++n) { bgv[n] = *(const LAS f32x4*)(bg + 4 * n); blv[n] = *(const LAS f32x4*)(bl + 4 * n); }
;         constexpr float SC = 1.f / (QS_X1 * QS_WUP);
; #pragma unroll
;         for (int ai = 0; ai < 2; ++ai)
; #pragma unroll
;             for (int m = 0; m < 4; ++m) { unsigned char* rowp = H + (size_t)(row0 + ai * 128 + m * 16) * DM + col0; u32x2 w;
; #pragma unroll
;                 for (int n = 0; n < 2; ++n) { const f32x4 g = acc[ai][0][m][n] * SC + bgv[n], l = acc[ai][1][m][n] * SC + blv[n];
;                     const f32x2 o0 = act2((f32x2){g[0], g[1]}, (f32x2){l[0], l[1]}), o1 = act2((f32x2){g[2], g[3]}, (f32x2){l[2], l[3]});
;                     int r = 0; r = __builtin_amdgcn_cvt_pk_fp8_f32(e2m3q<EMU_DOWN != 0>(o0.x), e2m3q<EMU_DOWN != 0>(o0.y), r, false); r = __builtin_amdgcn_cvt_pk_fp8_f32(e2m3q<EMU_DOWN != 0>(o1.x), e2m3q<EMU_DOWN != 0>(o1.y), r, true);
;                     if (n == 0) w.x = (unsigned)r; else w.y = (unsigned)r; }
;                 *(u32x2*)rowp = w; }
	s_nop 0
	v_rcp_f32_e32 v172, v172
	v_rcp_f32_e32 v173, v173
	s_nop 0
	v_pk_mul_f32 v[18:19], v[18:19], v[172:173]
	s_nop 0
	v_pk_mul_f32 v[18:19], v[22:23], v[18:19]
	v_cvt_pk_fp8_f32 v150, v20, v21
	v_pk_fma_f32 v[20:21], v[136:137], s[36:37], v[0:1] op_sel_hi:[1,0,1]
	v_min_f32_e32 v21, 0x40e00000, v21
	v_min_f32_e32 v20, 0x40e00000, v20
	v_pk_mul_f32 v[176:177], v[20:21], s[78:79] op_sel_hi:[1,0]
	v_cvt_pk_fp8_f32 v150, v18, v19 op_sel:[0,0,1]
	v_exp_f32_e32 v176, v176
	v_exp_f32_e32 v177, v177
	v_pk_fma_f32 v[18:19], v[138:139], s[36:37], v[2:3] op_sel_hi:[1,0,1]
	v_pk_fma_f32 v[172:173], v[106:107], s[36:37], v[6:7] op_sel_hi:[1,0,1]
	v_min_f32_e32 v19, 0x40e00000, v19
	v_pk_add_f32 v[176:177], v[176:177], 1.0 op_sel_hi:[1,0]
	v_min_f32_e32 v18, 0x40e00000, v18
	v_rcp_f32_e32 v176, v176
	v_rcp_f32_e32 v177, v177
	v_med3_f32 v173, v173, s47, v190
	v_med3_f32 v172, v172, s47, v190
	v_pk_fma_f32 v[172:173], v[172:173], 4.0, 4.0 op_sel_hi:[1,0,0]
	v_pk_mul_f32 v[20:21], v[20:21], v[176:177]
	s_nop 0
	v_pk_mul_f32 v[20:21], v[174:175], v[20:21]
	v_pk_mul_f32 v[174:175], v[18:19], s[78:79] op_sel_hi:[1,0]
	v_cvt_pk_fp8_f32 v151, v20, v21
	v_exp_f32_e32 v174, v174
	v_exp_f32_e32 v175, v175
	v_pk_fma_f32 v[20:21], v[132:133], s[36:37], v[8:9] op_sel_hi:[1,0,1]
	v_pk_add_f32 v[174:175], v[174:175], 1.0 op_sel_hi:[1,0]
	s_nop 0
	v_rcp_f32_e32 v174, v174
	v_rcp_f32_e32 v175, v175
	v_min_f32_e32 v21, 0x40e00000, v21
	v_min_f32_e32 v20, 0x40e00000, v20
	v_pk_mul_f32 v[18:19], v[18:19], v[174:175]
	v_pk_mul_f32 v[174:175], v[20:21], s[78:79] op_sel_hi:[1,0]
	v_pk_mul_f32 v[18:19], v[172:173], v[18:19]
	v_exp_f32_e32 v174, v174
	v_exp_f32_e32 v175, v175
	v_cvt_pk_fp8_f32 v151, v18, v19 op_sel:[0,0,1]
	v_add_co_u32_e32 v18, vcc, s20, v16
	v_pk_add_f32 v[174:175], v[174:175], 1.0 op_sel_hi:[1,0]
	s_nop 0
	v_addc_co_u32_e32 v19, vcc, 0, v17, vcc
	v_rcp_f32_e32 v174, v174
	v_rcp_f32_e32 v175, v175
	v_pk_fma_f32 v[172:173], v[100:101], s[36:37], v[12:13] op_sel_hi:[1,0,1]
	v_permlane16_swap_b32_e32 v148, v150
	v_permlane16_swap_b32_e32 v149, v151
	global_store_dwordx4 v[144:145], v[148:151], off
	v_pk_fma_f32 v[18:19], v[134:135], s[36:37], v[10:11] op_sel_hi:[1,0,1]
	v_med3_f32 v173, v173, s47, v190
	v_med3_f32 v172, v172, s47, v190
	v_pk_mul_f32 v[20:21], v[20:21], v[174:175]
	v_pk_fma_f32 v[172:173], v[172:173], 4.0, 4.0 op_sel_hi:[1,0,0]
	v_min_f32_e32 v19, 0x40e00000, v19
	v_min_f32_e32 v18, 0x40e00000, v18
	v_pk_mul_f32 v[20:21], v[172:173], v[20:21]
	v_pk_mul_f32 v[172:173], v[18:19], s[78:79] op_sel_hi:[1,0]
	v_pk_fma_f32 v[22:23], v[102:103], s[36:37], v[14:15] op_sel_hi:[1,0,1]
	v_exp_f32_e32 v172, v172
	v_exp_f32_e32 v173, v173
	v_med3_f32 v23, v23, s47, v190
	v_med3_f32 v22, v22, s47, v190
	v_pk_fma_f32 v[22:23], v[22:23], 4.0, 4.0 op_sel_hi:[1,0,0]
	v_pk_add_f32 v[172:173], v[172:173], 1.0 op_sel_hi:[1,0]
	v_pk_fma_f32 v[174:175], v[96:97], s[36:37], v[4:5] op_sel_hi:[1,0,1]
	v_rcp_f32_e32 v172, v172
	v_rcp_f32_e32 v173, v173
	v_med3_f32 v175, v175, s47, v190
	v_med3_f32 v174, v174, s47, v190
	v_pk_fma_f32 v[174:175], v[174:175], 4.0, 4.0 op_sel_hi:[1,0,0]
	v_pk_mul_f32 v[18:19], v[18:19], v[172:173]
	v_pk_fma_f32 v[172:173], v[98:99], s[36:37], v[6:7] op_sel_hi:[1,0,1]
	v_pk_mul_f32 v[18:19], v[22:23], v[18:19]
	v_cvt_pk_fp8_f32 v148, v20, v21
	v_pk_fma_f32 v[20:21], v[128:129], s[36:37], v[0:1] op_sel_hi:[1,0,1]
	v_min_f32_e32 v21, 0x40e00000, v21
	v_min_f32_e32 v20, 0x40e00000, v20
	v_pk_mul_f32 v[176:177], v[20:21], s[78:79] op_sel_hi:[1,0]
	v_cvt_pk_fp8_f32 v148, v18, v19 op_sel:[0,0,1]
	v_exp_f32_e32 v176, v176
	v_exp_f32_e32 v177, v177
	v_pk_fma_f32 v[18:19], v[130:131], s[36:37], v[2:3] op_sel_hi:[1,0,1]
	v_med3_f32 v173, v173, s47, v190
	v_min_f32_e32 v19, 0x40e00000, v19
	v_pk_add_f32 v[176:177], v[176:177], 1.0 op_sel_hi:[1,0]
	v_min_f32_e32 v18, 0x40e00000, v18
	v_rcp_f32_e32 v176, v176
	v_rcp_f32_e32 v177, v177
	v_med3_f32 v172, v172, s47, v190
	v_pk_fma_f32 v[172:173], v[172:173], 4.0, 4.0 op_sel_hi:[1,0,0]
	s_mov_b32 s20, 0x8000
	v_pk_mul_f32 v[20:21], v[20:21], v[176:177]
	s_nop 0
	v_pk_mul_f32 v[20:21], v[174:175], v[20:21]
	v_pk_mul_f32 v[174:175], v[18:19], s[78:79] op_sel_hi:[1,0]
	v_cvt_pk_fp8_f32 v149, v20, v21
	v_exp_f32_e32 v174, v174
	v_exp_f32_e32 v175, v175
	v_pk_fma_f32 v[20:21], v[124:125], s[36:37], v[8:9] op_sel_hi:[1,0,1]
	v_pk_add_f32 v[174:175], v[174:175], 1.0 op_sel_hi:[1,0]
	s_nop 0
	v_rcp_f32_e32 v174, v174
	v_rcp_f32_e32 v175, v175
	v_min_f32_e32 v21, 0x40e00000, v21
	v_min_f32_e32 v20, 0x40e00000, v20
	v_pk_mul_f32 v[18:19], v[18:19], v[174:175]
	v_pk_mul_f32 v[174:175], v[20:21], s[78:79] op_sel_hi:[1,0]
	v_pk_mul_f32 v[18:19], v[172:173], v[18:19]
	v_exp_f32_e32 v174, v174
	v_exp_f32_e32 v175, v175
	v_cvt_pk_fp8_f32 v149, v18, v19 op_sel:[0,0,1]
	v_add_co_u32_e32 v18, vcc, s20, v16
	v_pk_add_f32 v[174:175], v[174:175], 1.0 op_sel_hi:[1,0]
	s_nop 0
	v_addc_co_u32_e32 v19, vcc, 0, v17, vcc
	v_rcp_f32_e32 v174, v174
	v_rcp_f32_e32 v175, v175
	v_pk_fma_f32 v[172:173], v[92:93], s[36:37], v[12:13] op_sel_hi:[1,0,1]
	v_lshl_add_u64 v[146:147], v[18:19], 0, v[152:153]
	v_pk_fma_f32 v[18:19], v[126:127], s[36:37], v[10:11] op_sel_hi:[1,0,1]
	v_med3_f32 v173, v173, s47, v190
	v_med3_f32 v172, v172, s47, v190
	v_pk_mul_f32 v[20:21], v[20:21], v[174:175]
	v_pk_fma_f32 v[172:173], v[172:173], 4.0, 4.0 op_sel_hi:[1,0,0]
	v_min_f32_e32 v19, 0x40e00000, v19
	v_min_f32_e32 v18, 0x40e00000, v18
	v_pk_mul_f32 v[20:21], v[172:173], v[20:21]
	v_pk_mul_f32 v[172:173], v[18:19], s[78:79] op_sel_hi:[1,0]
	v_pk_fma_f32 v[22:23], v[94:95], s[36:37], v[14:15] op_sel_hi:[1,0,1]
	v_exp_f32_e32 v172, v172
	v_exp_f32_e32 v173, v173
; #define LAS __attribute__((address_space(3)))
; template <bool EMU> __device__ __forceinline__ float e2m3q(float y) { if constexpr (EMU) { y = fminf(fmaxf(y, -7.5f), 7.5f); return fabsf(y) < 1.f ? rintf(y * 8.f) * 0.125f : y; } else return y; }
;     static __device__ __forceinline__ f32x2 act2(f32x2 g, f32x2 l) {
;         g = __builtin_elementwise_min(g, (f32x2){7.f, 7.f}); l = __builtin_elementwise_min(__builtin_elementwise_max(l, (f32x2){-7.f, -7.f}), (f32x2){7.f, 7.f});
;         const f32x2 t = g * (-1.702f * 1.44269504089f); f32x2 e; e.x = __builtin_amdgcn_exp2f(t.x); e.y = __builtin_amdgcn_exp2f(t.y);
;         const f32x2 d = e + 1.0f; f32x2 r; r.x = __builtin_amdgcn_rcpf(d.x); r.y = __builtin_amdgcn_rcpf(d.y);
;         return (g * r) * (l * QS_ACT + QS_ACT);
;     }
;     __device__ __forceinline__ void operator()(const f32x4 (&acc)[2][2][4][2], const UnitD& u, int wr, int wc, int fr, int fq) const {
;         const int row0 = u.r0 + wr * 64 + fr, col0 = u.c0 + wc * 32 + 8 * fq;
;         const LAS float* bg = bl_lds + u.ui * 256 + wc * 32 + 8 * fq; const LAS float* bl = bg + 128;
;         f32x4 bgv[2], blv[2];
; #pragma unroll
;         for (int n = 0; n < 2; ++n) { bgv[n] = *(const LAS f32x4*)(bg + 4 * n); blv[n] = *(const LAS f32x4*)(bl + 4 * n); }
;         constexpr float SC = 1.f / (QS_X1 * QS_WUP);
; #pragma unroll
;         for (int ai = 0; ai < 2; ++ai)
; #pragma unroll
;             for (int m = 0; m < 4; ++m) { unsigned char* rowp = H + (size_t)(row0 + ai * 128 + m * 16) * DM + col0; u32x2 w;
; #pragma unroll
;                 for (int n = 0; n < 2; ++n) { const f32x4 g = acc[ai][0][m][n] * SC + bgv[n], l = acc[ai][1][m][n] * SC + blv[n];
;                     const f32x2 o0 = act2((f32x2){g[0], g[1]}, (f32x2){l[0], l[1]}), o1 = act2((f32x2){g[2], g[3]}, (f32x2){l[2], l[3]});
;                     int r = 0; r = __builtin_amdgcn_cvt_pk_fp8_f32(e2m3q<EMU_DOWN != 0>(o0.x), e2m3q<EMU_DOWN != 0>(o0.y), r, false); r = __builtin_amdgcn_cvt_pk_fp8_f32(e2m3q<EMU_DOWN != 0>(o1.x), e2m3q<EMU_DOWN != 0>(o1.y), r, true);
;                     if (n == 0) w.x = (unsigned)r; else w.y = (unsigned)r; }
;                 *(u32x2*)rowp = w; }
	v_med3_f32 v23, v23, s47, v190
	v_med3_f32 v22, v22, s47, v190
	v_pk_fma_f32 v[22:23], v[22:23], 4.0, 4.0 op_sel_hi:[1,0,0]
	v_pk_add_f32 v[172:173], v[172:173], 1.0 op_sel_hi:[1,0]
	v_pk_fma_f32 v[174:175], v[88:89], s[36:37], v[4:5] op_sel_hi:[1,0,1]
	v_rcp_f32_e32 v172, v172
	v_rcp_f32_e32 v173, v173
	v_med3_f32 v175, v175, s47, v190
	v_med3_f32 v174, v174, s47, v190
	v_pk_fma_f32 v[174:175], v[174:175], 4.0, 4.0 op_sel_hi:[1,0,0]
	v_pk_mul_f32 v[18:19], v[18:19], v[172:173]
	v_pk_fma_f32 v[172:173], v[90:91], s[36:37], v[6:7] op_sel_hi:[1,0,1]
	v_pk_mul_f32 v[18:19], v[22:23], v[18:19]
	v_cvt_pk_fp8_f32 v150, v20, v21
	v_pk_fma_f32 v[20:21], v[120:121], s[36:37], v[0:1] op_sel_hi:[1,0,1]
	v_min_f32_e32 v21, 0x40e00000, v21
	v_min_f32_e32 v20, 0x40e00000, v20
	v_pk_mul_f32 v[176:177], v[20:21], s[78:79] op_sel_hi:[1,0]
	v_cvt_pk_fp8_f32 v150, v18, v19 op_sel:[0,0,1]
	v_exp_f32_e32 v176, v176
	v_exp_f32_e32 v177, v177
	v_pk_fma_f32 v[18:19], v[122:123], s[36:37], v[2:3] op_sel_hi:[1,0,1]
	v_med3_f32 v173, v173, s47, v190
	v_min_f32_e32 v19, 0x40e00000, v19
	v_pk_add_f32 v[176:177], v[176:177], 1.0 op_sel_hi:[1,0]
	v_min_f32_e32 v18, 0x40e00000, v18
	v_rcp_f32_e32 v176, v176
	v_rcp_f32_e32 v177, v177
	v_med3_f32 v172, v172, s47, v190
	v_pk_fma_f32 v[172:173], v[172:173], 4.0, 4.0 op_sel_hi:[1,0,0]
	s_mov_b32 s20, 0xc000
	v_pk_mul_f32 v[20:21], v[20:21], v[176:177]
	s_nop 0
	v_pk_mul_f32 v[20:21], v[174:175], v[20:21]
	v_pk_mul_f32 v[174:175], v[18:19], s[78:79] op_sel_hi:[1,0]
	v_cvt_pk_fp8_f32 v151, v20, v21
	v_exp_f32_e32 v174, v174
	v_exp_f32_e32 v175, v175
	v_pk_fma_f32 v[20:21], v[84:85], s[36:37], v[8:9] op_sel_hi:[1,0,1]
	v_pk_add_f32 v[174:175], v[174:175], 1.0 op_sel_hi:[1,0]
	s_nop 0
	v_rcp_f32_e32 v174, v174
	v_rcp_f32_e32 v175, v175
	v_min_f32_e32 v21, 0x40e00000, v21
	v_min_f32_e32 v20, 0x40e00000, v20
	v_pk_mul_f32 v[18:19], v[18:19], v[174:175]
	v_pk_mul_f32 v[174:175], v[20:21], s[78:79] op_sel_hi:[1,0]
	v_pk_mul_f32 v[18:19], v[172:173], v[18:19]
	v_exp_f32_e32 v174, v174
	v_exp_f32_e32 v175, v175
	v_cvt_pk_fp8_f32 v151, v18, v19 op_sel:[0,0,1]
	v_add_co_u32_e32 v18, vcc, s20, v16
	v_pk_add_f32 v[174:175], v[174:175], 1.0 op_sel_hi:[1,0]
	s_nop 0
	v_addc_co_u32_e32 v19, vcc, 0, v17, vcc
	v_rcp_f32_e32 v174, v174
	v_rcp_f32_e32 v175, v175
	v_pk_fma_f32 v[172:173], v[52:53], s[36:37], v[12:13] op_sel_hi:[1,0,1]
	v_permlane16_swap_b32_e32 v148, v150
	v_permlane16_swap_b32_e32 v149, v151
	global_store_dwordx4 v[146:147], v[148:151], off
	v_pk_fma_f32 v[18:19], v[86:87], s[36:37], v[10:11] op_sel_hi:[1,0,1]
	v_med3_f32 v173, v173, s47, v190
	v_med3_f32 v172, v172, s47, v190
	v_pk_mul_f32 v[20:21], v[20:21], v[174:175]
	v_pk_fma_f32 v[172:173], v[172:173], 4.0, 4.0 op_sel_hi:[1,0,0]
	v_min_f32_e32 v19, 0x40e00000, v19
	v_min_f32_e32 v18, 0x40e00000, v18
	v_pk_mul_f32 v[20:21], v[172:173], v[20:21]
	v_pk_mul_f32 v[172:173], v[18:19], s[78:79] op_sel_hi:[1,0]
	v_pk_fma_f32 v[22:23], v[54:55], s[36:37], v[14:15] op_sel_hi:[1,0,1]
	v_exp_f32_e32 v172, v172
	v_exp_f32_e32 v173, v173
	v_med3_f32 v23, v23, s47, v190
	v_med3_f32 v22, v22, s47, v190
	v_pk_fma_f32 v[22:23], v[22:23], 4.0, 4.0 op_sel_hi:[1,0,0]
	v_pk_add_f32 v[172:173], v[172:173], 1.0 op_sel_hi:[1,0]
	v_pk_fma_f32 v[174:175], v[48:49], s[36:37], v[4:5] op_sel_hi:[1,0,1]
	v_rcp_f32_e32 v172, v172
	v_rcp_f32_e32 v173, v173
	v_med3_f32 v175, v175, s47, v190
	v_med3_f32 v174, v174, s47, v190
	v_pk_fma_f32 v[174:175], v[174:175], 4.0, 4.0 op_sel_hi:[1,0,0]
	v_pk_mul_f32 v[18:19], v[18:19], v[172:173]
	v_pk_fma_f32 v[172:173], v[50:51], s[36:37], v[6:7] op_sel_hi:[1,0,1]
	v_pk_mul_f32 v[18:19], v[22:23], v[18:19]
	v_cvt_pk_fp8_f32 v148, v20, v21
	v_pk_fma_f32 v[20:21], v[80:81], s[36:37], v[0:1] op_sel_hi:[1,0,1]
	v_min_f32_e32 v21, 0x40e00000, v21
	v_min_f32_e32 v20, 0x40e00000, v20
	v_pk_mul_f32 v[176:177], v[20:21], s[78:79] op_sel_hi:[1,0]
	v_cvt_pk_fp8_f32 v148, v18, v19 op_sel:[0,0,1]
	v_exp_f32_e32 v176, v176
	v_exp_f32_e32 v177, v177
	v_pk_fma_f32 v[18:19], v[82:83], s[36:37], v[2:3] op_sel_hi:[1,0,1]
	v_med3_f32 v173, v173, s47, v190
	v_min_f32_e32 v19, 0x40e00000, v19
	v_pk_add_f32 v[176:177], v[176:177], 1.0 op_sel_hi:[1,0]
	v_min_f32_e32 v18, 0x40e00000, v18
	v_rcp_f32_e32 v176, v176
	v_rcp_f32_e32 v177, v177
	v_med3_f32 v172, v172, s47, v190
	v_pk_fma_f32 v[172:173], v[172:173], 4.0, 4.0 op_sel_hi:[1,0,0]
	s_mov_b32 s20, 0x20000
	v_pk_mul_f32 v[20:21], v[20:21], v[176:177]
	s_nop 0
	v_pk_mul_f32 v[20:21], v[174:175], v[20:21]
	v_pk_mul_f32 v[174:175], v[18:19], s[78:79] op_sel_hi:[1,0]
	v_cvt_pk_fp8_f32 v149, v20, v21
	v_exp_f32_e32 v174, v174
	v_exp_f32_e32 v175, v175
	v_pk_fma_f32 v[20:21], v[76:77], s[36:37], v[8:9] op_sel_hi:[1,0,1]
	v_pk_add_f32 v[174:175], v[174:175], 1.0 op_sel_hi:[1,0]
	s_nop 0
	v_rcp_f32_e32 v174, v174
	v_rcp_f32_e32 v175, v175
	v_min_f32_e32 v21, 0x40e00000, v21
	v_min_f32_e32 v20, 0x40e00000, v20
	v_pk_mul_f32 v[18:19], v[18:19], v[174:175]
	v_pk_mul_f32 v[174:175], v[20:21], s[78:79] op_sel_hi:[1,0]
	v_pk_mul_f32 v[18:19], v[172:173], v[18:19]
	v_exp_f32_e32 v174, v174
	v_exp_f32_e32 v175, v175
	v_cvt_pk_fp8_f32 v149, v18, v19 op_sel:[0,0,1]
	v_add_co_u32_e32 v18, vcc, s20, v16
	v_pk_add_f32 v[174:175], v[174:175], 1.0 op_sel_hi:[1,0]
	s_nop 0
	v_addc_co_u32_e32 v19, vcc, 0, v17, vcc
	v_rcp_f32_e32 v174, v174
	v_rcp_f32_e32 v175, v175
	v_pk_fma_f32 v[172:173], v[44:45], s[36:37], v[12:13] op_sel_hi:[1,0,1]
	v_lshl_add_u64 v[146:147], v[18:19], 0, v[152:153]
	v_pk_fma_f32 v[18:19], v[78:79], s[36:37], v[10:11] op_sel_hi:[1,0,1]
	v_med3_f32 v173, v173, s47, v190
	v_med3_f32 v172, v172, s47, v190
	v_pk_mul_f32 v[20:21], v[20:21], v[174:175]
; #define LAS __attribute__((address_space(3)))
; template <bool EMU> __device__ __forceinline__ float e2m3q(float y) { if constexpr (EMU) { y = fminf(fmaxf(y, -7.5f), 7.5f); return fabsf(y) < 1.f ? rintf(y * 8.f) * 0.125f : y; } else return y; }
;     static __device__ __forceinline__ f32x2 act2(f32x2 g, f32x2 l) {
;         g = __builtin_elementwise_min(g, (f32x2){7.f, 7.f}); l = __builtin_elementwise_min(__builtin_elementwise_max(l, (f32x2){-7.f, -7.f}), (f32x2){7.f, 7.f});
;         const f32x2 t = g * (-1.702f * 1.44269504089f); f32x2 e; e.x = __builtin_amdgcn_exp2f(t.x); e.y = __builtin_amdgcn_exp2f(t.y);
;         const f32x2 d = e + 1.0f; f32x2 r; r.x = __builtin_amdgcn_rcpf(d.x); r.y = __builtin_amdgcn_rcpf(d.y);
;         return (g * r) * (l * QS_ACT + QS_ACT);
;     }
;     __device__ __forceinline__ void operator()(const f32x4 (&acc)[2][2][4][2], const UnitD& u, int wr, int wc, int fr, int fq) const {
;         const int row0 = u.r0 + wr * 64 + fr, col0 = u.c0 + wc * 32 + 8 * fq;
;         const LAS float* bg = bl_lds + u.ui * 256 + wc * 32 + 8 * fq; const LAS float* bl = bg + 128;
;         f32x4 bgv[2], blv[2];
; #pragma unroll
;         for (int n = 0; n < 2; ++n) { bgv[n] = *(const LAS f32x4*)(bg + 4 * n); blv[n] = *(const LAS f32x4*)(bl + 4 * n); }
;         constexpr float SC = 1.f / (QS_X1 * QS_WUP);
; #pragma unroll
;         for (int ai = 0; ai < 2; ++ai)
; #pragma unroll
;             for (int m = 0; m < 4; ++m) { unsigned char* rowp = H + (size_t)(row0 + ai * 128 + m * 16) * DM + col0; u32x2 w;
; #pragma unroll
;                 for (int n = 0; n < 2; ++n) { const f32x4 g = acc[ai][0][m][n] * SC + bgv[n], l = acc[ai][1][m][n] * SC + blv[n];
;                     const f32x2 o0 = act2((f32x2){g[0], g[1]}, (f32x2){l[0], l[1]}), o1 = act2((f32x2){g[2], g[3]}, (f32x2){l[2], l[3]});
;                     int r = 0; r = __builtin_amdgcn_cvt_pk_fp8_f32(e2m3q<EMU_DOWN != 0>(o0.x), e2m3q<EMU_DOWN != 0>(o0.y), r, false); r = __builtin_amdgcn_cvt_pk_fp8_f32(e2m3q<EMU_DOWN != 0>(o1.x), e2m3q<EMU_DOWN != 0>(o1.y), r, true);
;                     if (n == 0) w.x = (unsigned)r; else w.y = (unsigned)r; }
;                 *(u32x2*)rowp = w; }
	v_pk_fma_f32 v[172:173], v[172:173], 4.0, 4.0 op_sel_hi:[1,0,0]
	v_min_f32_e32 v19, 0x40e00000, v19
	v_min_f32_e32 v18, 0x40e00000, v18
	v_pk_mul_f32 v[20:21], v[172:173], v[20:21]
	v_pk_mul_f32 v[172:173], v[18:19], s[78:79] op_sel_hi:[1,0]
	v_pk_fma_f32 v[22:23], v[46:47], s[36:37], v[14:15] op_sel_hi:[1,0,1]
	v_exp_f32_e32 v172, v172
	v_exp_f32_e32 v173, v173
	v_med3_f32 v23, v23, s47, v190
	v_med3_f32 v22, v22, s47, v190
	v_pk_fma_f32 v[22:23], v[22:23], 4.0, 4.0 op_sel_hi:[1,0,0]
	v_pk_add_f32 v[172:173], v[172:173], 1.0 op_sel_hi:[1,0]
	v_pk_fma_f32 v[174:175], v[40:41], s[36:37], v[4:5] op_sel_hi:[1,0,1]
	v_rcp_f32_e32 v172, v172
	v_rcp_f32_e32 v173, v173
	v_med3_f32 v175, v175, s47, v190
	v_med3_f32 v174, v174, s47, v190
	v_pk_fma_f32 v[174:175], v[174:175], 4.0, 4.0 op_sel_hi:[1,0,0]
	v_pk_mul_f32 v[18:19], v[18:19], v[172:173]
	v_pk_fma_f32 v[172:173], v[42:43], s[36:37], v[6:7] op_sel_hi:[1,0,1]
	v_pk_mul_f32 v[18:19], v[22:23], v[18:19]
	v_cvt_pk_fp8_f32 v150, v20, v21
	v_pk_fma_f32 v[20:21], v[72:73], s[36:37], v[0:1] op_sel_hi:[1,0,1]
	v_min_f32_e32 v21, 0x40e00000, v21
	v_min_f32_e32 v20, 0x40e00000, v20
	v_pk_mul_f32 v[176:177], v[20:21], s[78:79] op_sel_hi:[1,0]
	v_cvt_pk_fp8_f32 v150, v18, v19 op_sel:[0,0,1]
	v_exp_f32_e32 v176, v176
	v_exp_f32_e32 v177, v177
	v_pk_fma_f32 v[18:19], v[74:75], s[36:37], v[2:3] op_sel_hi:[1,0,1]
	v_med3_f32 v173, v173, s47, v190
	v_min_f32_e32 v19, 0x40e00000, v19
	v_pk_add_f32 v[176:177], v[176:177], 1.0 op_sel_hi:[1,0]
	v_min_f32_e32 v18, 0x40e00000, v18
	v_rcp_f32_e32 v176, v176
	v_rcp_f32_e32 v177, v177
	v_med3_f32 v172, v172, s47, v190
	v_pk_fma_f32 v[172:173], v[172:173], 4.0, 4.0 op_sel_hi:[1,0,0]
	s_mov_b32 s20, 0x24000
	v_pk_mul_f32 v[20:21], v[20:21], v[176:177]
	s_nop 0
	v_pk_mul_f32 v[20:21], v[174:175], v[20:21]
	v_pk_mul_f32 v[174:175], v[18:19], s[78:79] op_sel_hi:[1,0]
	v_cvt_pk_fp8_f32 v151, v20, v21
	v_exp_f32_e32 v174, v174
	v_exp_f32_e32 v175, v175
	v_pk_fma_f32 v[20:21], v[68:69], s[36:37], v[8:9] op_sel_hi:[1,0,1]
	v_pk_fma_f32 v[8:9], v[60:61], s[36:37], v[8:9] op_sel_hi:[1,0,1]
	v_min_f32_e32 v21, 0x40e00000, v21
	v_pk_add_f32 v[174:175], v[174:175], 1.0 op_sel_hi:[1,0]
	v_min_f32_e32 v20, 0x40e00000, v20
	v_rcp_f32_e32 v174, v174
	v_rcp_f32_e32 v175, v175
	v_min_f32_e32 v9, 0x40e00000, v9
	v_min_f32_e32 v8, 0x40e00000, v8
	v_pk_mul_f32 v[18:19], v[18:19], v[174:175]
	v_pk_mul_f32 v[174:175], v[20:21], s[78:79] op_sel_hi:[1,0]
	v_pk_mul_f32 v[18:19], v[172:173], v[18:19]
	v_exp_f32_e32 v174, v174
	v_exp_f32_e32 v175, v175
	v_cvt_pk_fp8_f32 v151, v18, v19 op_sel:[0,0,1]
	v_add_co_u32_e32 v18, vcc, s20, v16
	v_pk_add_f32 v[174:175], v[174:175], 1.0 op_sel_hi:[1,0]
	s_nop 0
	v_addc_co_u32_e32 v19, vcc, 0, v17, vcc
	v_rcp_f32_e32 v174, v174
	v_rcp_f32_e32 v175, v175
	v_pk_fma_f32 v[172:173], v[36:37], s[36:37], v[12:13] op_sel_hi:[1,0,1]
	v_permlane16_swap_b32_e32 v148, v150
	v_permlane16_swap_b32_e32 v149, v151
	global_store_dwordx4 v[146:147], v[148:151], off
	v_pk_fma_f32 v[18:19], v[70:71], s[36:37], v[10:11] op_sel_hi:[1,0,1]
	v_med3_f32 v173, v173, s47, v190
	v_med3_f32 v172, v172, s47, v190
	v_pk_mul_f32 v[20:21], v[20:21], v[174:175]
	v_pk_fma_f32 v[172:173], v[172:173], 4.0, 4.0 op_sel_hi:[1,0,0]
	v_min_f32_e32 v19, 0x40e00000, v19
	v_min_f32_e32 v18, 0x40e00000, v18
	v_pk_mul_f32 v[20:21], v[172:173], v[20:21]
	v_pk_mul_f32 v[172:173], v[18:19], s[78:79] op_sel_hi:[1,0]
	v_pk_fma_f32 v[22:23], v[38:39], s[36:37], v[14:15] op_sel_hi:[1,0,1]
	v_exp_f32_e32 v172, v172
	v_exp_f32_e32 v173, v173
	v_med3_f32 v23, v23, s47, v190
	v_med3_f32 v22, v22, s47, v190
	v_pk_fma_f32 v[22:23], v[22:23], 4.0, 4.0 op_sel_hi:[1,0,0]
	v_pk_add_f32 v[172:173], v[172:173], 1.0 op_sel_hi:[1,0]
	v_pk_fma_f32 v[174:175], v[32:33], s[36:37], v[4:5] op_sel_hi:[1,0,1]
	v_rcp_f32_e32 v172, v172
	v_rcp_f32_e32 v173, v173
	v_med3_f32 v175, v175, s47, v190
	v_med3_f32 v174, v174, s47, v190
	v_pk_fma_f32 v[174:175], v[174:175], 4.0, 4.0 op_sel_hi:[1,0,0]
	v_pk_mul_f32 v[18:19], v[18:19], v[172:173]
	v_pk_fma_f32 v[172:173], v[34:35], s[36:37], v[6:7] op_sel_hi:[1,0,1]
	v_pk_mul_f32 v[18:19], v[22:23], v[18:19]
	v_cvt_pk_fp8_f32 v148, v20, v21
	v_pk_fma_f32 v[20:21], v[64:65], s[36:37], v[0:1] op_sel_hi:[1,0,1]
; #define LAS __attribute__((address_space(3)))
; template <bool EMU> __device__ __forceinline__ float e2m3q(float y) { if constexpr (EMU) { y = fminf(fmaxf(y, -7.5f), 7.5f); return fabsf(y) < 1.f ? rintf(y * 8.f) * 0.125f : y; } else return y; }
;     static __device__ __forceinline__ f32x2 act2(f32x2 g, f32x2 l) {
;         g = __builtin_elementwise_min(g, (f32x2){7.f, 7.f}); l = __builtin_elementwise_min(__builtin_elementwise_max(l, (f32x2){-7.f, -7.f}), (f32x2){7.f, 7.f});
;         const f32x2 t = g * (-1.702f * 1.44269504089f); f32x2 e; e.x = __builtin_amdgcn_exp2f(t.x); e.y = __builtin_amdgcn_exp2f(t.y);
;         const f32x2 d = e + 1.0f; f32x2 r; r.x = __builtin_amdgcn_rcpf(d.x); r.y = __builtin_amdgcn_rcpf(d.y);
;         return (g * r) * (l * QS_ACT + QS_ACT);
;     }
;     __device__ __forceinline__ void operator()(const f32x4 (&acc)[2][2][4][2], const UnitD& u, int wr, int wc, int fr, int fq) const {
;         const int row0 = u.r0 + wr * 64 + fr, col0 = u.c0 + wc * 32 + 8 * fq;
;         const LAS float* bg = bl_lds + u.ui * 256 + wc * 32 + 8 * fq; const LAS float* bl = bg + 128;
;         f32x4 bgv[2], blv[2];
; #pragma unroll
;         for (int n = 0; n < 2; ++n) { bgv[n] = *(const LAS f32x4*)(bg + 4 * n); blv[n] = *(const LAS f32x4*)(bl + 4 * n); }
;         constexpr float SC = 1.f / (QS_X1 * QS_WUP);
; #pragma unroll
;         for (int ai = 0; ai < 2; ++ai)
; #pragma unroll
;             for (int m = 0; m < 4; ++m) { unsigned char* rowp = H + (size_t)(row0 + ai * 128 + m * 16) * DM + col0; u32x2 w;
; #pragma unroll
;                 for (int n = 0; n < 2; ++n) { const f32x4 g = acc[ai][0][m][n] * SC + bgv[n], l = acc[ai][1][m][n] * SC + blv[n];
;                     const f32x2 o0 = act2((f32x2){g[0], g[1]}, (f32x2){l[0], l[1]}), o1 = act2((f32x2){g[2], g[3]}, (f32x2){l[2], l[3]});
;                     int r = 0; r = __builtin_amdgcn_cvt_pk_fp8_f32(e2m3q<EMU_DOWN != 0>(o0.x), e2m3q<EMU_DOWN != 0>(o0.y), r, false); r = __builtin_amdgcn_cvt_pk_fp8_f32(e2m3q<EMU_DOWN != 0>(o1.x), e2m3q<EMU_DOWN != 0>(o1.y), r, true);
;                     if (n == 0) w.x = (unsigned)r; else w.y = (unsigned)r; }
;                 *(u32x2*)rowp = w; }
	v_min_f32_e32 v21, 0x40e00000, v21
	v_min_f32_e32 v20, 0x40e00000, v20
	v_pk_mul_f32 v[176:177], v[20:21], s[78:79] op_sel_hi:[1,0]
	v_cvt_pk_fp8_f32 v148, v18, v19 op_sel:[0,0,1]
	v_exp_f32_e32 v176, v176
	v_exp_f32_e32 v177, v177
	v_pk_fma_f32 v[18:19], v[66:67], s[36:37], v[2:3] op_sel_hi:[1,0,1]
	v_med3_f32 v173, v173, s47, v190
	v_min_f32_e32 v19, 0x40e00000, v19
	v_pk_add_f32 v[176:177], v[176:177], 1.0 op_sel_hi:[1,0]
	v_min_f32_e32 v18, 0x40e00000, v18
	v_rcp_f32_e32 v176, v176
	v_rcp_f32_e32 v177, v177
	v_med3_f32 v172, v172, s47, v190
	v_pk_fma_f32 v[172:173], v[172:173], 4.0, 4.0 op_sel_hi:[1,0,0]
	s_mov_b32 s20, 0x28000
	v_pk_mul_f32 v[20:21], v[20:21], v[176:177]
	v_pk_fma_f32 v[12:13], v[28:29], s[36:37], v[12:13] op_sel_hi:[1,0,1]
	v_pk_mul_f32 v[20:21], v[174:175], v[20:21]
	v_pk_mul_f32 v[174:175], v[18:19], s[78:79] op_sel_hi:[1,0]
	v_cvt_pk_fp8_f32 v149, v20, v21
	v_exp_f32_e32 v174, v174
	v_exp_f32_e32 v175, v175
	v_pk_fma_f32 v[10:11], v[62:63], s[36:37], v[10:11] op_sel_hi:[1,0,1]
	v_med3_f32 v13, v13, s47, v190
	v_med3_f32 v12, v12, s47, v190
	v_pk_add_f32 v[174:175], v[174:175], 1.0 op_sel_hi:[1,0]
	v_pk_fma_f32 v[14:15], v[30:31], s[36:37], v[14:15] op_sel_hi:[1,0,1]
	v_rcp_f32_e32 v174, v174
	v_rcp_f32_e32 v175, v175
	v_pk_fma_f32 v[12:13], v[12:13], 4.0, 4.0 op_sel_hi:[1,0,0]
	v_min_f32_e32 v11, 0x40e00000, v11
	v_min_f32_e32 v10, 0x40e00000, v10
	v_pk_mul_f32 v[18:19], v[18:19], v[174:175]
	v_pk_fma_f32 v[0:1], v[56:57], s[36:37], v[0:1] op_sel_hi:[1,0,1]
	v_pk_mul_f32 v[18:19], v[172:173], v[18:19]
	v_min_f32_e32 v1, 0x40e00000, v1
	v_cvt_pk_fp8_f32 v149, v18, v19 op_sel:[0,0,1]
	v_add_co_u32_e32 v18, vcc, s20, v16
	v_min_f32_e32 v0, 0x40e00000, v0
	s_nop 0
	v_addc_co_u32_e32 v19, vcc, 0, v17, vcc
	v_lshl_add_u64 v[146:147], v[18:19], 0, v[152:153]
	v_pk_mul_f32 v[18:19], v[8:9], s[78:79] op_sel_hi:[1,0]
	v_pk_fma_f32 v[4:5], v[24:25], s[36:37], v[4:5] op_sel_hi:[1,0,1]
	v_exp_f32_e32 v18, v18
	v_exp_f32_e32 v19, v19
	v_pk_fma_f32 v[2:3], v[58:59], s[36:37], v[2:3] op_sel_hi:[1,0,1]
	v_med3_f32 v5, v5, s47, v190
	v_med3_f32 v4, v4, s47, v190
	v_pk_add_f32 v[18:19], v[18:19], 1.0 op_sel_hi:[1,0]
	v_pk_fma_f32 v[6:7], v[26:27], s[36:37], v[6:7] op_sel_hi:[1,0,1]
	v_rcp_f32_e32 v18, v18
	v_rcp_f32_e32 v19, v19
	v_pk_fma_f32 v[4:5], v[4:5], 4.0, 4.0 op_sel_hi:[1,0,0]
	v_min_f32_e32 v3, 0x40e00000, v3
	v_min_f32_e32 v2, 0x40e00000, v2
	v_pk_mul_f32 v[8:9], v[8:9], v[18:19]
	s_nop 0
	v_pk_mul_f32 v[8:9], v[12:13], v[8:9]
	v_med3_f32 v13, v15, s47, v190
	v_med3_f32 v12, v14, s47, v190
	v_pk_mul_f32 v[14:15], v[10:11], s[78:79] op_sel_hi:[1,0]
	v_pk_fma_f32 v[12:13], v[12:13], 4.0, 4.0 op_sel_hi:[1,0,0]
	v_exp_f32_e32 v14, v14
	v_exp_f32_e32 v15, v15
	s_nop 0
	v_pk_add_f32 v[14:15], v[14:15], 1.0 op_sel_hi:[1,0]
	s_nop 0
	v_rcp_f32_e32 v14, v14
	v_rcp_f32_e32 v15, v15
	s_nop 0
	v_pk_mul_f32 v[10:11], v[10:11], v[14:15]
	s_nop 0
	v_pk_mul_f32 v[10:11], v[12:13], v[10:11]
	v_cvt_pk_fp8_f32 v150, v8, v9
	v_pk_mul_f32 v[8:9], v[0:1], s[78:79] op_sel_hi:[1,0]
	v_exp_f32_e32 v8, v8
	v_exp_f32_e32 v9, v9
	v_cvt_pk_fp8_f32 v150, v10, v11 op_sel:[0,0,1]
	v_pk_add_f32 v[8:9], v[8:9], 1.0 op_sel_hi:[1,0]
	s_nop 0
	v_rcp_f32_e32 v8, v8
	v_rcp_f32_e32 v9, v9
	s_nop 0
	v_pk_mul_f32 v[0:1], v[0:1], v[8:9]
	s_nop 0
	v_pk_mul_f32 v[0:1], v[4:5], v[0:1]
	v_med3_f32 v5, v7, s47, v190
	v_med3_f32 v4, v6, s47, v190
	v_pk_mul_f32 v[6:7], v[2:3], s[78:79] op_sel_hi:[1,0]
	v_cvt_pk_fp8_f32 v151, v0, v1
	v_exp_f32_e32 v6, v6
	v_exp_f32_e32 v7, v7
	v_pk_fma_f32 v[4:5], v[4:5], 4.0, 4.0 op_sel_hi:[1,0,0]
	v_add_co_u32_e32 v0, vcc, 0x2c000, v16
	v_pk_add_f32 v[6:7], v[6:7], 1.0 op_sel_hi:[1,0]
	s_nop 0
	v_addc_co_u32_e32 v1, vcc, 0, v17, vcc
	v_rcp_f32_e32 v6, v6
	v_rcp_f32_e32 v7, v7
	s_andn2_b64 vcc, exec, s[16:17]
	v_pk_mul_f32 v[2:3], v[2:3], v[6:7]
	s_nop 0
	v_pk_mul_f32 v[2:3], v[4:5], v[2:3]
	s_nop 0
	v_cvt_pk_fp8_f32 v151, v2, v3 op_sel:[0,0,1]
	s_nop 1
	v_permlane16_swap_b32_e32 v148, v150
	v_permlane16_swap_b32_e32 v149, v151
	global_store_dwordx4 v[146:147], v[148:151], off
	s_cbranch_vccnz .LBB0_759
	s_andn2_b64 vcc, exec, s[4:5]
	s_mov_b32 s86, 0x2f9636c4
	s_cbranch_vccnz .LBB0_758
	s_barrier
